# adds GEMM prologues: second K-tile staging loads issued with the first tile's (one wait less at phase start)
# baseline (speedup 1.0000x reference)
; #define PG8_STAGE(bufoff, gbase, voff) do { _Pragma("unroll") for (int _i = 0; _i < 2; ++_i) \
;         __builtin_amdgcn_global_load_lds((const unsigned*)((const char*)(gbase) + (voff)[_i]), (PG8_LAS unsigned*)(lds + (bufoff) + ldsw + _i * 8192), 16, 0, 0); } while (0)
; #define PG8_WAIT_V(n) asm volatile("s_waitcnt vmcnt(" #n ")" ::: "memory")
; #define PG8_BAR __builtin_amdgcn_s_barrier()
; template <class Epi, class Sched, bool ALIGN_EPI = false, bool SP2 = false, bool F8 = false, bool GATHER = false>
; __device__ __forceinline__ void gemm_phase(PG8_LAS unsigned char* lds, const Gemm g, const Sched& S, const Epi& E) {
;     ...
;         PG8_STAGE(PG8_SB(0, 0), cB, voffB); PG8_STAGE(PG8_SB(0, 1), cB + hstep, voffB); PG8_STAGE(PG8_SA(0, 0), cA, vo[0]); PG8_STAGE(PG8_SA(0, 1), cA, vo[1]);
;         if (wr == 1) PG8_BAR;
;         PG8_WAIT_V(2); PG8_BAR;
;         PG8_STAGE(PG8_SB(1, 0), cB + kstep, voffB); PG8_STAGE(PG8_SA(1, 0), cA + kstep, vo[0]); PG8_STAGE(PG8_SB(1, 1), cB + hstep + kstep, voffB);
;         PG8_WAIT_V(6); PG8_BAR;
.LBB0_117:
	s_add_u32 s54, s30, 0x6000000
	s_addc_u32 s55, s31, 0
	s_lshl_b32 s9, s9, 5
	s_mov_b64 s[58:59], 0x80
	s_and_b32 s56, s9, 0x60
	s_add_i32 m0, s11, 0x18000
	v_lshl_add_u64 v[8:9], v[8:9], 0, s[58:59]
	s_lshl_b32 s7, s8, 13
	s_lshl_b32 s9, s56, 7
	global_load_lds_dwordx4 v[8:9], off
	v_lshl_add_u64 v[6:7], v[6:7], 0, s[58:59]
	s_add_i32 m0, s11, 0x1a000
	s_add_i32 s36, s11, 0x8000
	s_add_i32 s37, s11, 0xa000
	global_load_lds_dwordx4 v[6:7], off
	v_lshl_add_u64 v[2:3], v[2:3], 0, s[58:59]
	s_mov_b32 m0, s36
	s_add_u32 s40, s82, 0x40080
	global_load_lds_dwordx4 v[2:3], off
	v_lshl_add_u64 v[2:3], v[4:5], 0, s[58:59]
	s_mov_b32 m0, s37
	s_addc_u32 s41, s83, 0
	global_load_lds_dwordx4 v[2:3], off
	s_add_i32 m0, s11, 0x1c000
	v_lshl_add_u64 v[2:3], s[40:41], 0, v[164:165]
	global_load_lds_dwordx4 v[2:3], off
	v_lshl_add_u64 v[2:3], s[40:41], 0, v[168:169]
	s_add_i32 m0, s11, 0x1e000
	s_cmpk_lt_u32 s38, 0x100
	global_load_lds_dwordx4 v[2:3], off
	s_waitcnt vmcnt(8)
	s_barrier
	v_lshrrev_b32_e32 v3, 1, v10
	v_and_b32_e32 v176, 24, v3
	v_and_b32_e32 v2, 15, v10
	v_lshlrev_b32_e32 v3, 1, v176
	v_lshl_or_b32 v195, s8, 6, v2
	v_lshl_or_b32 v2, v2, 6, v3
	v_lshlrev_b32_e32 v3, 2, v10
	v_and_b32_e32 v3, 32, v3
	v_bitop3_b32 v4, v2, s7, v3 bitop3:0xde
	v_bitop3_b32 v196, v2, s9, v3 bitop3:0xde
	v_lshlrev_b32_e32 v2, 14, v14
	v_and_b32_e32 v2, 0xffff8000, v2
	v_lshl_add_u32 v2, v15, 11, v2
	v_and_b32_e32 v3, 1, v14
	v_lshl_or_b32 v2, v3, 6, v2
	v_lshlrev_b32_e32 v3, 1, v16
	v_add3_u32 v178, v2, v3, s5
	v_lshlrev_b32_e32 v2, 14, v11
	v_and_b32_e32 v2, 0xffff8000, v2
	s_waitcnt vmcnt(6)
	v_lshl_add_u32 v2, v12, 11, v2
	v_and_b32_e32 v3, 1, v11
	s_cselect_b64 s[60:61], -1, 0
	v_lshl_or_b32 v2, v3, 6, v2
	v_lshlrev_b32_e32 v3, 1, v13
	s_add_i32 s40, 0, 0x10000
	s_add_i32 s41, 0, 0x14000
	s_mov_b32 s62, 0x76543210
	v_mov_b32_e32 v171, v175
	v_mov_b32_e32 v173, v175
	v_or_b32_e32 v197, s56, v176
	s_mov_b32 s57, s45
	v_mov_b32_e32 v177, v175
	s_ashr_i32 s38, s86, 31
	s_ashr_i32 s39, s91, 31
	v_mov_b32_e32 v179, v175
	v_add3_u32 v180, v2, v3, s5
	v_mov_b32_e32 v181, v175
	v_mov_b64_e32 v[182:183], 0x500
	v_mov_b64_e32 v[184:185], 0x4ff
	v_add_u32_e32 v198, s40, v196
	v_add_u32_e32 v199, s41, v196
	v_add_u32_e32 v200, 0, v4
	v_mov_b32_e32 v201, 0x7f7f7f7f
	s_movk_i32 s63, 0x98
	s_movk_i32 s48, 0x5000
	s_mov_b32 s70, 0x3c800000
	s_movk_i32 s49, 0xb800
	s_mov_b32 s50, 0
	s_barrier
	s_branch .LBB0_120

; #define PG8_STAGE(bufoff, gbase, voff) do { _Pragma("unroll") for (int _i = 0; _i < 2; ++_i) \
;         __builtin_amdgcn_global_load_lds((const unsigned*)((const char*)(gbase) + (voff)[_i]), (PG8_LAS unsigned*)(lds + (bufoff) + ldsw + _i * 8192), 16, 0, 0); } while (0)
; #define PG8_WAIT_V(n) asm volatile("s_waitcnt vmcnt(" #n ")" ::: "memory")
; #define PG8_BAR __builtin_amdgcn_s_barrier()
; template <class Epi, class Sched, bool ALIGN_EPI = false, bool SP2 = false, bool F8 = false, bool GATHER = false>
; __device__ __forceinline__ void gemm_phase(PG8_LAS unsigned char* lds, const Gemm g, const Sched& S, const Epi& E) {
;     ...
;         PG8_STAGE(PG8_SB(0, 0), cB, voffB); PG8_STAGE(PG8_SB(0, 1), cB + hstep, voffB); PG8_STAGE(PG8_SA(0, 0), cA, vo[0]); PG8_STAGE(PG8_SA(0, 1), cA, vo[1]);
;         if (wr == 1) PG8_BAR;
;         PG8_WAIT_V(2); PG8_BAR;
;         PG8_STAGE(PG8_SB(1, 0), cB + kstep, voffB); PG8_STAGE(PG8_SA(1, 0), cA + kstep, vo[0]); PG8_STAGE(PG8_SB(1, 1), cB + hstep + kstep, voffB);
;         PG8_WAIT_V(6); PG8_BAR;
.LBB0_720:
	s_add_u32 s36, s30, 0x6003000
	s_addc_u32 s37, s31, 0
	s_lshl_b32 s38, s38, 5
	s_and_b32 s46, s38, 0x60
	s_mov_b64 s[38:39], 0x80
	s_add_i32 m0, s48, 0x18000
	v_lshl_add_u64 v[8:9], v[8:9], 0, s[38:39]
	s_lshl_b32 s41, s40, 13
	s_lshl_b32 s47, s46, 7
	global_load_lds_dwordx4 v[8:9], off
	v_lshl_add_u64 v[6:7], v[6:7], 0, s[38:39]
	s_add_i32 m0, s48, 0x1a000
	s_add_i32 s52, s48, 0x8000
	s_add_i32 s53, s48, 0xa000
	global_load_lds_dwordx4 v[6:7], off
	v_lshl_add_u64 v[2:3], v[2:3], 0, s[38:39]
	s_mov_b32 m0, s52
	s_add_u32 s44, s62, 0x20080
	global_load_lds_dwordx4 v[2:3], off
	v_lshl_add_u64 v[2:3], v[4:5], 0, s[38:39]
	s_mov_b32 m0, s53
	s_addc_u32 s45, s63, 0
	global_load_lds_dwordx4 v[2:3], off
	s_add_i32 m0, s48, 0x1c000
	v_lshl_add_u64 v[2:3], s[44:45], 0, v[166:167]
	global_load_lds_dwordx4 v[2:3], off
	v_lshl_add_u64 v[2:3], s[44:45], 0, v[162:163]
	s_add_i32 m0, s48, 0x1e000
	s_cmpk_lt_u32 s5, 0x100
	global_load_lds_dwordx4 v[2:3], off
	s_waitcnt vmcnt(8)
	s_barrier
	v_lshrrev_b32_e32 v3, 1, v10
	v_and_b32_e32 v3, 24, v3
	v_and_b32_e32 v2, 15, v10
	v_lshlrev_b32_e32 v4, 1, v3
	v_lshl_or_b32 v191, s40, 6, v2
	v_lshl_or_b32 v2, v2, 6, v4
	v_lshlrev_b32_e32 v4, 2, v10
	v_and_b32_e32 v4, 32, v4
	v_bitop3_b32 v5, v2, s41, v4 bitop3:0xde
	v_bitop3_b32 v192, v2, s47, v4 bitop3:0xde
	v_lshlrev_b32_e32 v2, 13, v11
	v_and_b32_e32 v2, 0xffffc000, v2
	v_or_b32_e32 v193, s46, v3
	v_lshl_add_u32 v2, v12, 10, v2
	v_and_b32_e32 v3, 1, v11
	v_lshl_or_b32 v2, v3, 6, v2
	v_lshlrev_b32_e32 v3, 1, v13
	v_add3_u32 v174, v2, v3, s42
	v_lshlrev_b32_e32 v2, 13, v15
	v_and_b32_e32 v2, 0xffffc000, v2
	s_waitcnt vmcnt(6)
	v_lshl_add_u32 v2, v14, 10, v2
	v_and_b32_e32 v3, 1, v15
	s_cselect_b64 s[40:41], -1, 0
	v_lshl_or_b32 v2, v3, 6, v2
	v_lshlrev_b32_e32 v3, 1, v16
	s_add_i32 s66, 0, 0x10000
	s_add_i32 s67, 0, 0x14000
	v_mov_b32_e32 v171, v167
	v_mov_b32_e32 v173, v167
	s_sext_i32_i8 s69, s4
	s_mov_b32 s59, 0
	v_mov_b32_e32 v175, v167
	v_add3_u32 v176, v2, v3, s42
	v_mov_b32_e32 v177, v167
	v_mov_b64_e32 v[178:179], 0x100
	v_mov_b64_e32 v[180:181], 0xff
	v_add_u32_e32 v195, s66, v192
	v_add_u32_e32 v196, s67, v192
	v_add_u32_e32 v197, 0, v5
	v_mov_b32_e32 v198, 0x7f7f7f7f
	s_movk_i32 s68, 0x5000
	s_mov_b32 s42, 0x3a800000
	s_barrier
	s_branch .LBB0_723

; #define PG8_STAGE(bufoff, gbase, voff) do { _Pragma("unroll") for (int _i = 0; _i < 2; ++_i) \
;         __builtin_amdgcn_global_load_lds((const unsigned*)((const char*)(gbase) + (voff)[_i]), (PG8_LAS unsigned*)(lds + (bufoff) + ldsw + _i * 8192), 16, 0, 0); } while (0)
; #define PG8_WAIT_V(n) asm volatile("s_waitcnt vmcnt(" #n ")" ::: "memory")
; #define PG8_BAR __builtin_amdgcn_s_barrier()
; template <class Epi, class Sched, bool ALIGN_EPI = false, bool SP2 = false, bool F8 = false, bool GATHER = false>
; __device__ __forceinline__ void gemm_phase(PG8_LAS unsigned char* lds, const Gemm g, const Sched& S, const Epi& E) {
;     ...
;     if constexpr (SP2) {
;         PG8_STAGE(PG8_SB(0, 0), cB, voffB); PG8_STAGE(PG8_SB(0, 1), cB + hstep, voffB); PG8_STAGE(PG8_SA(0, 0), cA, vo[0]); PG8_STAGE(PG8_SA(0, 1), cA, vo[1]);
;         if (wr == 1) PG8_BAR;
;         PG8_WAIT_V(2); PG8_BAR;
;         PG8_STAGE(PG8_SB(1, 0), cB + kstep, voffB); PG8_STAGE(PG8_SA(1, 0), cA + kstep, vo[0]); PG8_STAGE(PG8_SB(1, 1), cB + hstep + kstep, voffB);
;         PG8_WAIT_V(6); PG8_BAR;
.LBB0_740:
	s_lshl_b32 s18, s18, 5
	s_and_b32 s44, s18, 0x60
	s_lshl_b32 s39, s38, 13
	s_lshl_b32 s45, s44, 7
	s_add_u32 s18, s30, 0x6004000
	s_addc_u32 s19, s31, 0
	s_add_u32 s22, s30, 0x20200000
	s_mov_b64 s[36:37], 0x80
	s_addc_u32 s23, s31, 0
	s_add_i32 m0, s34, 0x18000
	v_lshl_add_u64 v[8:9], v[8:9], 0, s[36:37]
	global_load_lds_dwordx4 v[8:9], off
	v_lshl_add_u64 v[6:7], v[6:7], 0, s[36:37]
	s_add_i32 m0, s34, 0x1a000
	s_add_i32 s50, s34, 0x8000
	s_add_i32 s51, s34, 0xa000
	global_load_lds_dwordx4 v[6:7], off
	v_lshl_add_u64 v[2:3], v[2:3], 0, s[36:37]
	s_mov_b32 m0, s50
	s_add_u32 s42, s60, 0x20080
	global_load_lds_dwordx4 v[2:3], off
	v_lshl_add_u64 v[2:3], v[4:5], 0, s[36:37]
	s_mov_b32 m0, s51
	s_addc_u32 s43, s61, 0
	global_load_lds_dwordx4 v[2:3], off
	s_add_i32 m0, s34, 0x1c000
	v_lshl_add_u64 v[2:3], s[42:43], 0, v[166:167]
	global_load_lds_dwordx4 v[2:3], off
	v_lshl_add_u64 v[2:3], s[42:43], 0, v[162:163]
	s_add_i32 m0, s34, 0x1e000
	s_cmpk_lt_u32 s5, 0x100
	global_load_lds_dwordx4 v[2:3], off
	s_waitcnt vmcnt(8)
	s_barrier
	v_lshrrev_b32_e32 v3, 1, v10
	v_and_b32_e32 v3, 24, v3
	v_and_b32_e32 v2, 15, v10
	v_lshlrev_b32_e32 v4, 1, v3
	v_lshl_or_b32 v191, s38, 6, v2
	v_lshl_or_b32 v2, v2, 6, v4
	v_lshlrev_b32_e32 v4, 2, v10
	v_and_b32_e32 v4, 32, v4
	v_bitop3_b32 v5, v2, s39, v4 bitop3:0xde
	v_bitop3_b32 v192, v2, s45, v4 bitop3:0xde
	v_lshlrev_b32_e32 v2, 13, v11
	v_and_b32_e32 v2, 0xffffc000, v2
	v_or_b32_e32 v193, s44, v3
	v_lshl_add_u32 v2, v12, 10, v2
	v_and_b32_e32 v3, 1, v11
	v_lshl_or_b32 v2, v3, 6, v2
	v_lshlrev_b32_e32 v3, 1, v13
	v_add3_u32 v174, v2, v3, s40
	v_lshlrev_b32_e32 v2, 13, v15
	v_and_b32_e32 v2, 0xffffc000, v2
	s_waitcnt vmcnt(6)
	v_lshl_add_u32 v2, v14, 10, v2
	v_and_b32_e32 v3, 1, v15
	s_cselect_b64 s[38:39], -1, 0
	v_lshl_or_b32 v2, v3, 6, v2
	v_lshlrev_b32_e32 v3, 1, v16
	s_add_i32 s52, 0, 0x10000
	s_add_i32 s53, 0, 0x14000
	v_mov_b32_e32 v171, v167
	v_mov_b32_e32 v173, v167
	s_sext_i32_i8 s64, s4
	v_mov_b32_e32 v175, v167
	v_add3_u32 v176, v2, v3, s40
	v_mov_b32_e32 v177, v167
	v_mov_b64_e32 v[178:179], 0x100
	v_mov_b64_e32 v[180:181], 0xff
	v_add_u32_e32 v195, s52, v192
	v_add_u32_e32 v196, s53, v192
	v_add_u32_e32 v197, 0, v5
	v_mov_b32_e32 v198, 0x7f7f7f7f
	s_movk_i32 s57, 0x5000
	s_mov_b32 s40, 0x3a800000
	s_barrier
	s_branch .LBB0_743

; #define PG8_STAGE(bufoff, gbase, voff) do { _Pragma("unroll") for (int _i = 0; _i < 2; ++_i) \
;         __builtin_amdgcn_global_load_lds((const unsigned*)((const char*)(gbase) + (voff)[_i]), (PG8_LAS unsigned*)(lds + (bufoff) + ldsw + _i * 8192), 16, 0, 0); } while (0)
; #define PG8_WAIT_V(n) asm volatile("s_waitcnt vmcnt(" #n ")" ::: "memory")
; #define PG8_BAR __builtin_amdgcn_s_barrier()
; template <class Epi, class Sched, bool ALIGN_EPI = false, bool SP2 = false, bool F8 = false, bool GATHER = false>
; __device__ __forceinline__ void gemm_phase(PG8_LAS unsigned char* lds, const Gemm g, const Sched& S, const Epi& E) {
;     ...
;     if constexpr (SP2) {
;         PG8_STAGE(PG8_SB(0, 0), cB, voffB); PG8_STAGE(PG8_SB(0, 1), cB + hstep, voffB); PG8_STAGE(PG8_SA(0, 0), cA, vo[0]); PG8_STAGE(PG8_SA(0, 1), cA, vo[1]);
;         if (wr == 1) PG8_BAR;
;         PG8_WAIT_V(2); PG8_BAR;
;         PG8_STAGE(PG8_SB(1, 0), cB + kstep, voffB); PG8_STAGE(PG8_SA(1, 0), cA + kstep, vo[0]); PG8_STAGE(PG8_SB(1, 1), cB + hstep + kstep, voffB);
;         PG8_WAIT_V(6); PG8_BAR;
.LBB0_815:
	s_add_u32 s14, s30, 0x22200000
	s_addc_u32 s15, s31, 0
	s_add_u32 s49, s30, 0x104000
	s_addc_u32 s50, s31, 0
	s_lshl_b32 s18, s18, 5
	s_and_b32 s40, s18, 0x60
	s_mov_b64 s[18:19], 0x80
	s_add_i32 m0, s33, 0x18000
	v_lshl_add_u64 v[8:9], v[8:9], 0, s[18:19]
	s_ashr_i32 s51, s86, 31
	s_lshl_b32 s23, s22, 13
	s_lshl_b32 s41, s40, 7
	global_load_lds_dwordx4 v[8:9], off
	v_lshl_add_u64 v[6:7], v[6:7], 0, s[18:19]
	s_add_i32 m0, s33, 0x1a000
	s_add_i32 s52, s33, 0x8000
	s_add_i32 s53, s33, 0xa000
	global_load_lds_dwordx4 v[6:7], off
	v_lshl_add_u64 v[2:3], v[2:3], 0, s[18:19]
	s_mov_b32 m0, s52
	s_add_u32 s38, s64, 0x40080
	global_load_lds_dwordx4 v[2:3], off
	v_lshl_add_u64 v[2:3], v[4:5], 0, s[18:19]
	s_mov_b32 m0, s53
	s_addc_u32 s39, s65, 0
	global_load_lds_dwordx4 v[2:3], off
	s_add_i32 m0, s33, 0x1c000
	v_lshl_add_u64 v[2:3], s[38:39], 0, v[164:165]
	global_load_lds_dwordx4 v[2:3], off
	v_lshl_add_u64 v[2:3], s[38:39], 0, v[162:163]
	s_add_i32 m0, s33, 0x1e000
	s_cmpk_lt_u32 s5, 0x100
	global_load_lds_dwordx4 v[2:3], off
	s_waitcnt vmcnt(8)
	s_barrier
	v_bfe_u32 v3, v10, 4, 2
	v_and_b32_e32 v2, 15, v10
	v_lshlrev_b32_e32 v4, 4, v3
	v_lshl_or_b32 v186, s22, 6, v2
	v_lshl_or_b32 v2, v2, 6, v4
	v_lshlrev_b32_e32 v4, 2, v10
	v_and_b32_e32 v4, 32, v4
	v_bitop3_b32 v5, v2, s23, v4 bitop3:0xde
	v_bitop3_b32 v187, v2, s41, v4 bitop3:0xde
	v_lshlrev_b32_e32 v2, 14, v11
	v_and_b32_e32 v2, 0xffff8000, v2
	v_lshl_or_b32 v188, v3, 2, s40
	v_lshl_add_u32 v2, v13, 11, v2
	v_and_b32_e32 v3, 1, v11
	v_lshl_or_b32 v2, v3, 6, v2
	v_lshlrev_b32_sdwa v3, v12, sext(v14) dst_sel:DWORD dst_unused:UNUSED_PAD src0_sel:DWORD src1_sel:WORD_0
	v_add3_u32 v170, v2, v3, s36
	v_lshlrev_b32_e32 v2, 14, v15
	v_and_b32_e32 v2, 0xffff8000, v2
	s_waitcnt vmcnt(6)
	v_lshl_add_u32 v2, v16, 11, v2
	v_and_b32_e32 v3, 1, v15
	s_cselect_b64 s[22:23], -1, 0
	v_lshl_or_b32 v2, v3, 6, v2
	v_lshlrev_b32_sdwa v3, v12, sext(v17) dst_sel:DWORD dst_unused:UNUSED_PAD src0_sel:DWORD src1_sel:WORD_0
	s_add_i32 s61, 0, 0x10000
	s_add_i32 s80, 0, 0x14000
	v_mov_b32_e32 v167, v165
	v_mov_b32_e32 v169, v165
	s_sext_i32_i8 s69, s4
	v_mov_b32_e32 v171, v165
	v_add3_u32 v172, v2, v3, s36
	v_mov_b32_e32 v173, v165
	v_mov_b64_e32 v[174:175], 0x100
	v_mov_b64_e32 v[176:177], 0xff
	v_add_u32_e32 v189, s61, v187
	v_add_u32_e32 v191, s80, v187
	v_add_u32_e32 v192, 0, v5
	v_mov_b32_e32 v193, 0x7f7f7f7f
	s_mov_b32 s36, 0x3a800000
	s_mov_b64 s[38:39], 0x100000
	s_mov_b64 s[40:41], 0x120000
	s_mov_b64 s[42:43], 0x140000
	s_mov_b64 s[44:45], 0x160000
	s_barrier
	s_branch .LBB0_818

; #define PG8_STAGE(bufoff, gbase, voff) do { _Pragma("unroll") for (int _i = 0; _i < 2; ++_i) \
;         __builtin_amdgcn_global_load_lds((const unsigned*)((const char*)(gbase) + (voff)[_i]), (PG8_LAS unsigned*)(lds + (bufoff) + ldsw + _i * 8192), 16, 0, 0); } while (0)
; #define PG8_WAIT_V(n) asm volatile("s_waitcnt vmcnt(" #n ")" ::: "memory")
; #define PG8_BAR __builtin_amdgcn_s_barrier()
; template <class Epi, class Sched, bool ALIGN_EPI = false, bool SP2 = false, bool F8 = false, bool GATHER = false>
; __device__ __forceinline__ void gemm_phase(PG8_LAS unsigned char* lds, const Gemm g, const Sched& S, const Epi& E) {
;     ...
;     if constexpr (SP2) {
;         PG8_STAGE(PG8_SB(0, 0), cB, voffB); PG8_STAGE(PG8_SB(0, 1), cB + hstep, voffB); PG8_STAGE(PG8_SA(0, 0), cA, vo[0]); PG8_STAGE(PG8_SA(0, 1), cA, vo[1]);
;         if (wr == 1) PG8_BAR;
;         PG8_WAIT_V(2); PG8_BAR;
;         PG8_STAGE(PG8_SB(1, 0), cB + kstep, voffB); PG8_STAGE(PG8_SA(1, 0), cA + kstep, vo[0]); PG8_STAGE(PG8_SB(1, 1), cB + hstep + kstep, voffB);
;         PG8_WAIT_V(6); PG8_BAR;
.LBB0_980:
	s_ashr_i32 s22, s86, 31
	s_lshl_b32 s5, s5, 5
	s_lshr_b32 s22, s22, 29
	s_and_b32 s5, s5, 0x60
	s_add_i32 s22, s86, s22
	s_lshl_b32 s41, s4, 13
	s_lshl_b32 s44, s5, 7
	s_ashr_i32 s35, s22, 3
	s_add_u32 s22, s30, 0x30200000
	s_addc_u32 s23, s31, 0
	s_add_u32 s36, s30, 0x4000080
	s_mov_b64 s[38:39], 0x80
	s_addc_u32 s37, s31, 0
	s_add_i32 m0, s9, 0x18000
	v_lshl_add_u64 v[4:5], v[4:5], 0, s[38:39]
	global_load_lds_dwordx4 v[4:5], off
	v_lshl_add_u64 v[2:3], v[2:3], 0, s[38:39]
	s_add_i32 m0, s9, 0x1a000
	s_add_i32 s47, s9, 0x8000
	s_add_i32 s54, s9, 0xa000
	global_load_lds_dwordx4 v[2:3], off
	v_lshl_add_u64 v[2:3], s[36:37], 0, v[162:163]
	s_mov_b32 m0, s47
	s_add_u32 s42, s48, 0x40080
	global_load_lds_dwordx4 v[2:3], off
	v_lshl_add_u64 v[2:3], s[36:37], 0, v[170:171]
	s_mov_b32 m0, s54
	s_addc_u32 s43, s49, 0
	global_load_lds_dwordx4 v[2:3], off
	s_add_i32 m0, s9, 0x1c000
	v_lshl_add_u64 v[2:3], s[42:43], 0, v[164:165]
	global_load_lds_dwordx4 v[2:3], off
	v_lshl_add_u64 v[2:3], s[42:43], 0, v[166:167]
	s_add_i32 m0, s9, 0x1e000
	s_cmpk_lt_u32 s40, 0x100
	global_load_lds_dwordx4 v[2:3], off
	s_waitcnt vmcnt(8)
	s_barrier
	v_lshrrev_b32_e32 v3, 1, v6
	v_and_b32_e32 v3, 24, v3
	v_and_b32_e32 v2, 15, v6
	v_lshlrev_b32_e32 v4, 1, v3
	v_lshl_or_b32 v171, s4, 6, v2
	v_lshl_or_b32 v2, v2, 6, v4
	v_lshlrev_b32_e32 v4, 2, v6
	v_and_b32_e32 v4, 32, v4
	s_waitcnt vmcnt(6)
	v_bitop3_b32 v5, v2, s41, v4 bitop3:0xde
	v_bitop3_b32 v194, v2, s44, v4 bitop3:0xde
	s_cselect_b64 s[40:41], -1, 0
	s_add_i32 s55, 0, 0x10000
	s_add_i32 s56, 0, 0x14000
	v_or_b32_e32 v195, s5, v3
	v_add_u32_e32 v196, s55, v194
	v_add_u32_e32 v197, s56, v194
	v_add_u32_e32 v198, 0, v5
	v_mov_b32_e32 v199, 0x7f7f7f7f
	s_mov_b32 s57, 0xc0e00000
	s_mov_b32 s58, 0x40000
	s_mov_b32 s59, 0x48000
	s_mov_b32 s60, 0x50000
	v_mov_b32_e32 v200, 0x40e00000
	v_mov_b32_e32 v205, v162
	s_barrier
	s_branch .LBB0_983

; #define PG8_STAGE(bufoff, gbase, voff) do { _Pragma("unroll") for (int _i = 0; _i < 2; ++_i) \
;         __builtin_amdgcn_global_load_lds((const unsigned*)((const char*)(gbase) + (voff)[_i]), (PG8_LAS unsigned*)(lds + (bufoff) + ldsw + _i * 8192), 16, 0, 0); } while (0)
; #define PG8_WAIT_V(n) asm volatile("s_waitcnt vmcnt(" #n ")" ::: "memory")
; #define PG8_BAR __builtin_amdgcn_s_barrier()
; template <class Epi, class Sched, bool ALIGN_EPI = false, bool SP2 = false, bool F8 = false, bool GATHER = false>
; __device__ __forceinline__ void gemm_phase(PG8_LAS unsigned char* lds, const Gemm g, const Sched& S, const Epi& E) {
;     ...
;     if constexpr (SP2) {
;         PG8_STAGE(PG8_SB(0, 0), cB, voffB); PG8_STAGE(PG8_SB(0, 1), cB + hstep, voffB); PG8_STAGE(PG8_SA(0, 0), cA, vo[0]); PG8_STAGE(PG8_SA(0, 1), cA, vo[1]);
;         if (wr == 1) PG8_BAR;
;         PG8_WAIT_V(2); PG8_BAR;
;         PG8_STAGE(PG8_SB(1, 0), cB + kstep, voffB); PG8_STAGE(PG8_SA(1, 0), cA + kstep, vo[0]); PG8_STAGE(PG8_SB(1, 1), cB + hstep + kstep, voffB);
;         PG8_WAIT_V(6); PG8_BAR;
.LBB0_1065:
	s_lshl_b32 s16, s16, 5
	s_and_b32 s40, s16, 0x60
	s_ashr_i32 s16, s86, 31
	s_lshr_b32 s16, s16, 29
	s_add_i32 s16, s86, s16
	s_lshl_b32 s38, s3, 13
	s_lshl_b32 s41, s40, 7
	s_ashr_i32 s53, s16, 3
	s_add_u32 s16, s30, 0x3a200000
	s_addc_u32 s17, s31, 0
	s_add_u32 s18, s30, 0x30200080
	s_addc_u32 s19, s31, 0
	s_cmp_lg_u64 s[24:25], 0
	s_mov_b64 s[22:23], 0x80
	s_cselect_b64 s[20:21], -1, 0
	s_add_i32 m0, s11, 0x18000
	v_lshl_add_u64 v[4:5], v[4:5], 0, s[22:23]
	global_load_lds_dwordx4 v[4:5], off
	v_lshl_add_u64 v[2:3], v[2:3], 0, s[22:23]
	s_add_i32 m0, s11, 0x1a000
	s_add_i32 s58, s11, 0x8000
	s_add_i32 s59, s11, 0xa000
	global_load_lds_dwordx4 v[2:3], off
	v_lshl_add_u64 v[2:3], s[18:19], 0, v[166:167]
	s_mov_b32 m0, s58
	s_add_u32 s36, s4, 0x40080
	global_load_lds_dwordx4 v[2:3], off
	v_lshl_add_u64 v[2:3], s[18:19], 0, v[168:169]
	s_mov_b32 m0, s59
	s_addc_u32 s37, s5, 0
	global_load_lds_dwordx4 v[2:3], off
	s_add_i32 m0, s11, 0x1c000
	v_lshl_add_u64 v[2:3], s[36:37], 0, v[164:165]
	global_load_lds_dwordx4 v[2:3], off
	v_lshl_add_u64 v[2:3], s[36:37], 0, v[162:163]
	s_add_i32 m0, s11, 0x1e000
	s_cmpk_lt_u32 s2, 0x100
	global_load_lds_dwordx4 v[2:3], off
	s_waitcnt vmcnt(8)
	s_barrier
	v_lshrrev_b32_e32 v3, 1, v6
	v_and_b32_e32 v3, 24, v3
	v_and_b32_e32 v2, 15, v6
	v_lshlrev_b32_e32 v4, 1, v3
	v_lshl_or_b32 v169, s3, 6, v2
	v_lshl_or_b32 v2, v2, 6, v4
	v_lshlrev_b32_e32 v4, 2, v6
	v_and_b32_e32 v4, 32, v4
	s_waitcnt vmcnt(6)
	v_bitop3_b32 v5, v2, s38, v4 bitop3:0xde
	v_bitop3_b32 v194, v2, s41, v4 bitop3:0xde
	s_cselect_b64 s[36:37], -1, 0
	s_add_i32 s60, 0, 0x10000
	s_add_i32 s61, 0, 0x14000
	v_or_b32_e32 v195, s40, v3
	v_add_u32_e32 v196, s60, v194
	v_add_u32_e32 v197, s61, v194
	v_add_u32_e32 v198, 0, v5
	v_mov_b32_e32 v199, 0x7f7f7f7f
	s_mov_b32 s38, 0x3c800000
	s_mov_b64 s[40:41], 0x80000
	s_mov_b32 s62, 0x80000
	s_mov_b64 s[42:43], 0x90000
	s_mov_b32 s63, 0x90000
	s_mov_b64 s[44:45], 0xa0000
	s_mov_b32 s64, 0xa0000
	s_mov_b64 s[46:47], 0xb0000
	s_mov_b32 s65, 0xb0000
	v_mov_b32_e32 v204, v166
	s_barrier
	s_branch .LBB0_1068
